# J: MoE-up: bias folded into accumulator init (next unit's bias prefetched at epilogue start), removing the bias-load round trip and 128 adds per unit from the epilogue
# speedup vs baseline: 1.0076x; 1.0076x over previous
; #define PG8_WAIT_V(n) asm volatile("s_waitcnt vmcnt(" #n ")" ::: "memory")
; template <class Epi, class Sched, bool ALIGN_EPI = false, bool SP2 = false, bool GATHER = false, bool HALFM = false>
; __device__ __forceinline__ void gemm_phase(PG8_LAS unsigned char* lds, const int Kdim, const Sched& S, const Epi& E) {
;     ...
;     f32x4 acc[2][2][4][2];
; #pragma unroll
;     for (int a = 0; a < 2; ++a)
; #pragma unroll
;         for (int b = 0; b < 2; ++b)
; #pragma unroll
;             for (int m = 0; m < 4; ++m)
; #pragma unroll
;                 for (int n = 0; n < 2; ++n) acc[a][b][m][n] = (f32x4){0.f, 0.f, 0.f, 0.f};
;     bf16x8 At[4][2], B0[2][2], B1[2][2];
;     const char* cA = cur.a; const char* cB = cur.b;
;     S.a_ready(cur);
;     const char* gA = nullptr; unsigned gc[2][2] = {{0u, 0u}, {0u, 0u}}, gn[2][2] = {{0u, 0u}, {0u, 0u}};
;     if constexpr (GATHER) { static_assert(SP2, "GATHER needs the SP2 loop"); gA = S.abase();
;         Unit u1; const bool h1 = S.next(1, u1);
; #pragma unroll
;         for (int h = 0; h < 2; ++h)
; #pragma unroll
;             for (int i = 0; i < 2; ++i) { gc[h][i] = (unsigned)S.row_index(cur, h * HALF + RA[i]) * (unsigned)(K * 2) + CA2[i]; gn[h][i] = h1 ? (unsigned)S.row_index(u1, h * HALF + RA[i]) * (unsigned)(K * 2) + CA2[i] : gc[h][i]; } }
;     if constexpr (SP2) {
;         PG8_STAGE(PG8_SB(0, 0), cB, voffB); PG8_STAGE(PG8_SB(0, 1), cB + hstep, voffB);
;         if constexpr (GATHER) { PG8_STAGE_G(PG8_SA(0, 0), 0, gc[0]); PG8_STAGE_G(PG8_SA(0, 1), 0, gc[1]); } else { PG8_STAGE(PG8_SA(0, 0), cA, voffA); PG8_STAGE(PG8_SA(0, 1), cA + hstep, voffA); }
;         if (wr == 1) PG8_BAR;
;         PG8_WAIT_V(2); PG8_BAR;
;         PG8_STAGE(PG8_SB(1, 0), cB + kstep, voffB); if constexpr (GATHER) PG8_STAGE_G(PG8_SA(1, 0), kstep, gc[0]); else PG8_STAGE(PG8_SA(1, 0), cA + kstep, voffA); PG8_STAGE(PG8_SB(1, 1), cB + hstep + kstep, voffB);
;         PG8_WAIT_V(6); PG8_BAR;
;     __device__ __forceinline__ void operator()(const pg8::f32x4 (&acc)[2][2][4][2], const pg8::Unit& u, int wr, int wc, int fr, int fq) const {
;     ...
;         const int colj = u.pn * 128 + wc * 32 + 8 * fq;
;         const float* bg = b_up + u.e * 2048 + colj;
;         f32x4 bgv[2], blv[2];
; #pragma unroll
;         for (int n = 0; n < 2; ++n) { bgv[n] = *(const f32x4*)(bg + 4 * n); blv[n] = *(const f32x4*)(bg + 1024 + 4 * n); }
.LBB0_1696:
	v_readlane_b32 s52, v251, 31
	s_lshl_b64 s[14:15], s[20:21], 18
	v_readlane_b32 s56, v251, 35
	v_bfe_u32 v9, v2, 4, 2
	v_readlane_b32 s57, v251, 36
	s_add_u32 s37, s56, s14
	v_and_b32_e32 v8, 15, v2
	v_lshlrev_b32_e32 v10, 3, v9
	v_lshlrev_b32_e32 v9, 4, v9
	v_lshlrev_b32_e32 v2, 2, v2
	s_addc_u32 s49, s57, s15
	s_and_b32 s7, s4, 3
	v_lshl_or_b32 v169, s5, 6, v8
	v_lshl_or_b32 v8, v8, 6, v9
	s_lshl_b32 s4, s5, 13
	v_and_b32_e32 v2, 32, v2
	v_bitop3_b32 v9, v8, s4, v2 bitop3:0xde
	s_lshl_b32 s4, s7, 12
	v_bitop3_b32 v170, v8, s4, v2 bitop3:0xde
	s_add_i32 m0, s12, 0x18000
	v_lshl_add_u64 v[4:5], v[4:5], 0, s[34:35]
	v_readlane_b32 s4, v251, 8
	v_mov_b32_e32 v149, v3
	s_waitcnt vmcnt(2)
	s_barrier
	global_load_lds_dwordx4 v[4:5], off
	v_lshl_add_u64 v[4:5], v[6:7], 0, s[34:35]
	s_add_i32 m0, s12, 0x1a000
	v_readlane_b32 s5, v251, 9
	s_add_i32 s50, s12, 0x8000
	v_mov_b32_e32 v151, v3
	global_load_lds_dwordx4 v[4:5], off
	v_lshl_add_u64 v[4:5], s[4:5], 0, v[148:149]
	s_mov_b32 m0, s50
	s_add_i32 s51, s12, 0xa000
	global_load_lds_dwordx4 v[4:5], off
	v_lshl_add_u64 v[4:5], s[4:5], 0, v[150:151]
	s_add_u32 s4, s40, 0x40080
	s_mov_b32 m0, s51
	s_addc_u32 s5, s41, 0
	global_load_lds_dwordx4 v[4:5], off
	s_add_i32 m0, s12, 0x1c000
	v_lshl_add_u64 v[4:5], s[4:5], 0, v[156:157]
	global_load_lds_dwordx4 v[4:5], off
	v_lshl_add_u64 v[4:5], s[4:5], 0, v[158:159]
	s_add_i32 m0, s12, 0x1e000
	s_cmpk_lt_u32 s6, 0x100
	global_load_lds_dwordx4 v[4:5], off
	s_waitcnt vmcnt(6)
	v_readlane_b32 s53, v251, 32
	v_readlane_b32 s54, v251, 33
	v_readlane_b32 s55, v251, 34
	v_lshl_or_b32 v149, s7, 5, v10
	s_cselect_b64 s[6:7], -1, 0
	s_lshl_b32 s4, s46, 11
	s_ashr_i32 s5, s4, 31
	s_lshl_b64 s[4:5], s[4:5], 2
	v_lshl_or_b32 v136, s47, 7, v149
	s_add_u32 s4, s37, s4
	s_addc_u32 s5, s49, s5
	v_ashrrev_i32_e32 v137, 31, v136
	v_lshl_add_u64 v[136:137], v[136:137], 2, s[4:5]
	global_load_dwordx4 v[224:227], v[136:137], off
	global_load_dwordx4 v[228:231], v[136:137], off offset:16
	s_mov_b64 s[4:5], 0x1000
	v_lshl_add_u64 v[138:139], v[136:137], 0, s[4:5]
	global_load_dwordx4 v[232:235], v[138:139], off
	global_load_dwordx4 v[236:239], v[138:139], off offset:16
	s_waitcnt vmcnt(0)
	v_mov_b32_e32 v4, v236
	v_or_b32_e32 v151, 16, v169
	v_or_b32_e32 v171, 32, v169
	v_or_b32_e32 v172, 48, v169
	v_add_u32_e32 v173, 0x80, v169
	v_add_u32_e32 v174, 0x90, v169
	v_add_u32_e32 v175, 0xa0, v169
	v_add_u32_e32 v176, 0xb0, v169
	s_mov_b32 s76, 0
	v_add_u32_e32 v177, 0, v9
	v_mov_b32_e32 v5, v237
	v_mov_b32_e32 v6, v238
	v_mov_b32_e32 v7, v239
	v_mov_b32_e32 v8, v232
	v_mov_b32_e32 v9, v233
	v_mov_b32_e32 v10, v234
	v_mov_b32_e32 v11, v235
	v_mov_b32_e32 v12, v236
	v_mov_b32_e32 v13, v237
	v_mov_b32_e32 v14, v238
	v_mov_b32_e32 v15, v239
	v_mov_b32_e32 v16, v232
	v_mov_b32_e32 v17, v233
	v_mov_b32_e32 v18, v234
	v_mov_b32_e32 v19, v235
	v_mov_b32_e32 v20, v236
	v_mov_b32_e32 v21, v237
	v_mov_b32_e32 v22, v238
	v_mov_b32_e32 v23, v239
	v_mov_b32_e32 v24, v232
	v_mov_b32_e32 v25, v233
	v_mov_b32_e32 v26, v234
	v_mov_b32_e32 v27, v235
	v_mov_b32_e32 v28, v236
	v_mov_b32_e32 v29, v237
	v_mov_b32_e32 v30, v238
	v_mov_b32_e32 v31, v239
	v_mov_b32_e32 v32, v232
	v_mov_b32_e32 v33, v233
	v_mov_b32_e32 v34, v234
	v_mov_b32_e32 v35, v235
	v_mov_b32_e32 v36, v228
	v_mov_b32_e32 v37, v229
	v_mov_b32_e32 v38, v230
	v_mov_b32_e32 v39, v231
	v_mov_b32_e32 v40, v224
	v_mov_b32_e32 v41, v225
	v_mov_b32_e32 v42, v226
	v_mov_b32_e32 v43, v227
	v_mov_b32_e32 v44, v228
	v_mov_b32_e32 v45, v229
	v_mov_b32_e32 v46, v230
	v_mov_b32_e32 v47, v231
	v_mov_b32_e32 v48, v224
	v_mov_b32_e32 v49, v225
	v_mov_b32_e32 v50, v226
	v_mov_b32_e32 v51, v227
	v_mov_b32_e32 v52, v228
	v_mov_b32_e32 v53, v229
	v_mov_b32_e32 v54, v230
	v_mov_b32_e32 v55, v231
	v_mov_b32_e32 v56, v224
	v_mov_b32_e32 v57, v225
	v_mov_b32_e32 v58, v226
	v_mov_b32_e32 v59, v227
	v_mov_b32_e32 v60, v228
	v_mov_b32_e32 v61, v229
	v_mov_b32_e32 v62, v230
	v_mov_b32_e32 v63, v231
	v_mov_b32_e32 v64, v224
	v_mov_b32_e32 v65, v225
	v_mov_b32_e32 v66, v226
	v_mov_b32_e32 v67, v227
	v_mov_b32_e32 v68, v236
	v_mov_b32_e32 v69, v237
	v_mov_b32_e32 v70, v238
	v_mov_b32_e32 v71, v239
	v_mov_b32_e32 v72, v232
	v_mov_b32_e32 v73, v233
	v_mov_b32_e32 v74, v234
	v_mov_b32_e32 v75, v235
	v_mov_b32_e32 v76, v236
	v_mov_b32_e32 v77, v237
	v_mov_b32_e32 v78, v238
	v_mov_b32_e32 v79, v239
	v_mov_b32_e32 v80, v232
	v_mov_b32_e32 v81, v233
	v_mov_b32_e32 v82, v234
	v_mov_b32_e32 v83, v235
	v_mov_b32_e32 v84, v236
	v_mov_b32_e32 v85, v237
	v_mov_b32_e32 v86, v238
	v_mov_b32_e32 v87, v239
	v_mov_b32_e32 v88, v232
	v_mov_b32_e32 v89, v233
	v_mov_b32_e32 v90, v234
	v_mov_b32_e32 v91, v235
	v_mov_b32_e32 v92, v236
	v_mov_b32_e32 v93, v237
	v_mov_b32_e32 v94, v238
	v_mov_b32_e32 v95, v239
	v_mov_b32_e32 v96, v232
	v_mov_b32_e32 v97, v233
	v_mov_b32_e32 v98, v234
	v_mov_b32_e32 v99, v235
	v_mov_b32_e32 v100, v228
	v_mov_b32_e32 v101, v229
	v_mov_b32_e32 v102, v230
	v_mov_b32_e32 v103, v231
	v_mov_b32_e32 v104, v224
	v_mov_b32_e32 v105, v225
	v_mov_b32_e32 v106, v226
	v_mov_b32_e32 v107, v227
	v_mov_b32_e32 v108, v228
	v_mov_b32_e32 v109, v229
	v_mov_b32_e32 v110, v230
	v_mov_b32_e32 v111, v231
	v_mov_b32_e32 v112, v224
	v_mov_b32_e32 v113, v225
	v_mov_b32_e32 v114, v226
	v_mov_b32_e32 v115, v227
	v_mov_b32_e32 v116, v228
	v_mov_b32_e32 v117, v229
	v_mov_b32_e32 v118, v230
	v_mov_b32_e32 v119, v231
	v_mov_b32_e32 v120, v224
	v_mov_b32_e32 v121, v225
	v_mov_b32_e32 v122, v226
	v_mov_b32_e32 v123, v227
	v_mov_b32_e32 v124, v228
	v_mov_b32_e32 v125, v229
	v_mov_b32_e32 v126, v230
	v_mov_b32_e32 v127, v231
	v_mov_b32_e32 v128, v224
	v_mov_b32_e32 v129, v225
	v_mov_b32_e32 v130, v226
	v_mov_b32_e32 v131, v227
	v_readlane_b32 s58, v251, 37
	v_readlane_b32 s59, v251, 38
	v_readlane_b32 s60, v251, 39
	v_readlane_b32 s61, v251, 40
	v_readlane_b32 s62, v251, 41
	v_readlane_b32 s63, v251, 42
	v_readlane_b32 s64, v251, 43
	v_readlane_b32 s65, v251, 44
	v_readlane_b32 s66, v251, 45
	v_readlane_b32 s67, v251, 46
	s_barrier
	s_branch .LBB0_1698
; #define PG8_BAR __builtin_amdgcn_s_barrier()
; template <class Epi, class Sched, bool ALIGN_EPI = false, bool SP2 = false, bool GATHER = false, bool HALFM = false>
; __device__ __forceinline__ void gemm_phase(PG8_LAS unsigned char* lds, const int Kdim, const Sched& S, const Epi& E) {
;     ...
;         if (!has_next) break;
; #pragma unroll
;         for (int a = 0; a < 2; ++a)
; #pragma unroll
;             for (int b = 0; b < 2; ++b)
; #pragma unroll
;                 for (int m = 0; m < 4; ++m)
; #pragma unroll
;                     for (int n = 0; n < 2; ++n) acc[a][b][m][n] = (f32x4){0.f, 0.f, 0.f, 0.f};
;         cur = nxt; cA = nA; cB = nB; ++ui;
;         if constexpr (GATHER) {
; #pragma unroll
;             for (int h = 0; h < 2; ++h)
; #pragma unroll
;                 for (int i = 0; i < 2; ++i) { gc[h][i] = gn[h][i]; if (has_nn) gn[h][i] = (unsigned)ix[h][i] * (unsigned)(K * 2) + CA2[i]; } }
;         if constexpr (ALIGN_EPI) { if (wr == 1) PG8_BAR; }
.LBB0_1697:
	v_lshlrev_b32_e32 v178, 11, v178
	v_lshlrev_b32_e32 v179, 11, v179
	v_lshlrev_b32_e32 v180, 11, v180
	v_lshlrev_b32_e32 v181, 11, v181
	v_add_u32_e32 v4, v178, v165
	v_cndmask_b32_e64 v5, v166, v4, s[42:43]
	v_add_u32_e32 v4, v181, v162
	v_add_u32_e32 v2, v179, v162
	v_cndmask_b32_e64 v6, v167, v4, s[42:43]
	v_add_u32_e32 v4, v180, v165
	v_cndmask_b32_e64 v2, v163, v2, s[42:43]
	v_cndmask_b32_e64 v7, v168, v4, s[42:43]
	s_waitcnt vmcnt(8)
	v_mov_b32_e32 v4, v236
	v_mov_b32_e32 v148, v163
	v_mov_b32_e32 v150, v166
	v_mov_b32_e32 v152, v167
	v_mov_b32_e32 v154, v168
	v_mov_b32_e32 v163, v2
	v_mov_b32_e32 v166, v5
	v_mov_b32_e32 v167, v6
	v_mov_b32_e32 v168, v7
	s_mov_b32 s48, s57
	s_mov_b32 s47, s54
	s_mov_b32 s46, s52
	s_mov_b64 s[40:41], s[16:17]
	v_mov_b32_e32 v5, v237
	v_mov_b32_e32 v6, v238
	v_mov_b32_e32 v7, v239
	v_mov_b32_e32 v8, v232
	v_mov_b32_e32 v9, v233
	v_mov_b32_e32 v10, v234
	v_mov_b32_e32 v11, v235
	v_mov_b32_e32 v12, v236
	v_mov_b32_e32 v13, v237
	v_mov_b32_e32 v14, v238
	v_mov_b32_e32 v15, v239
	v_mov_b32_e32 v16, v232
	v_mov_b32_e32 v17, v233
	v_mov_b32_e32 v18, v234
	v_mov_b32_e32 v19, v235
	v_mov_b32_e32 v20, v236
	v_mov_b32_e32 v21, v237
	v_mov_b32_e32 v22, v238
	v_mov_b32_e32 v23, v239
	v_mov_b32_e32 v24, v232
	v_mov_b32_e32 v25, v233
	v_mov_b32_e32 v26, v234
	v_mov_b32_e32 v27, v235
	v_mov_b32_e32 v28, v236
	v_mov_b32_e32 v29, v237
	v_mov_b32_e32 v30, v238
	v_mov_b32_e32 v31, v239
	v_mov_b32_e32 v32, v232
	v_mov_b32_e32 v33, v233
	v_mov_b32_e32 v34, v234
	v_mov_b32_e32 v35, v235
	v_mov_b32_e32 v36, v228
	v_mov_b32_e32 v37, v229
	v_mov_b32_e32 v38, v230
	v_mov_b32_e32 v39, v231
	v_mov_b32_e32 v40, v224
	v_mov_b32_e32 v41, v225
	v_mov_b32_e32 v42, v226
	v_mov_b32_e32 v43, v227
	v_mov_b32_e32 v44, v228
	v_mov_b32_e32 v45, v229
	v_mov_b32_e32 v46, v230
	v_mov_b32_e32 v47, v231
	v_mov_b32_e32 v48, v224
	v_mov_b32_e32 v49, v225
	v_mov_b32_e32 v50, v226
	v_mov_b32_e32 v51, v227
	v_mov_b32_e32 v52, v228
	v_mov_b32_e32 v53, v229
	v_mov_b32_e32 v54, v230
	v_mov_b32_e32 v55, v231
	v_mov_b32_e32 v56, v224
	v_mov_b32_e32 v57, v225
	v_mov_b32_e32 v58, v226
	v_mov_b32_e32 v59, v227
	v_mov_b32_e32 v60, v228
	v_mov_b32_e32 v61, v229
	v_mov_b32_e32 v62, v230
	v_mov_b32_e32 v63, v231
	v_mov_b32_e32 v64, v224
	v_mov_b32_e32 v65, v225
	v_mov_b32_e32 v66, v226
	v_mov_b32_e32 v67, v227
	v_mov_b32_e32 v68, v236
	v_mov_b32_e32 v69, v237
	v_mov_b32_e32 v70, v238
	v_mov_b32_e32 v71, v239
	v_mov_b32_e32 v72, v232
	v_mov_b32_e32 v73, v233
	v_mov_b32_e32 v74, v234
	v_mov_b32_e32 v75, v235
	v_mov_b32_e32 v76, v236
	v_mov_b32_e32 v77, v237
	v_mov_b32_e32 v78, v238
	v_mov_b32_e32 v79, v239
	v_mov_b32_e32 v80, v232
	v_mov_b32_e32 v81, v233
	v_mov_b32_e32 v82, v234
	v_mov_b32_e32 v83, v235
	v_mov_b32_e32 v84, v236
	v_mov_b32_e32 v85, v237
	v_mov_b32_e32 v86, v238
	v_mov_b32_e32 v87, v239
	v_mov_b32_e32 v88, v232
	v_mov_b32_e32 v89, v233
	v_mov_b32_e32 v90, v234
	v_mov_b32_e32 v91, v235
	v_mov_b32_e32 v92, v236
	v_mov_b32_e32 v93, v237
	v_mov_b32_e32 v94, v238
	v_mov_b32_e32 v95, v239
	v_mov_b32_e32 v96, v232
	v_mov_b32_e32 v97, v233
	v_mov_b32_e32 v98, v234
	v_mov_b32_e32 v99, v235
	v_mov_b32_e32 v100, v228
	v_mov_b32_e32 v101, v229
	v_mov_b32_e32 v102, v230
	v_mov_b32_e32 v103, v231
	v_mov_b32_e32 v104, v224
	v_mov_b32_e32 v105, v225
	v_mov_b32_e32 v106, v226
	v_mov_b32_e32 v107, v227
	v_mov_b32_e32 v108, v228
	v_mov_b32_e32 v109, v229
	v_mov_b32_e32 v110, v230
	v_mov_b32_e32 v111, v231
	v_mov_b32_e32 v112, v224
	v_mov_b32_e32 v113, v225
	v_mov_b32_e32 v114, v226
	v_mov_b32_e32 v115, v227
	v_mov_b32_e32 v116, v228
	v_mov_b32_e32 v117, v229
	v_mov_b32_e32 v118, v230
	v_mov_b32_e32 v119, v231
	v_mov_b32_e32 v120, v224
	v_mov_b32_e32 v121, v225
	v_mov_b32_e32 v122, v226
	v_mov_b32_e32 v123, v227
	v_mov_b32_e32 v124, v228
	v_mov_b32_e32 v125, v229
	v_mov_b32_e32 v126, v230
	v_mov_b32_e32 v127, v231
	v_mov_b32_e32 v128, v224
	v_mov_b32_e32 v129, v225
	v_mov_b32_e32 v130, v226
	v_mov_b32_e32 v131, v227
	s_mov_b32 s76, s77
	s_andn2_b64 vcc, exec, s[38:39]
	s_cbranch_vccz .LBB0_1723

; __device__ __forceinline__ unsigned cvt_pk_bf16(float lo, float hi) { unsigned r; asm volatile("v_cvt_pk_bf16_f32 %0, %1, %2" : "=v"(r) : "v"(lo), "v"(hi)); return r; }
;     __device__ __forceinline__ void operator()(const pg8::f32x4 (&acc)[2][2][4][2], const pg8::Unit& u, int wr, int wc, int fr, int fq) const {
;         const bool side = side_layer >= 0 && u.lx < 2304; const int sit = u.lx * 8 + wr * 4 + wc, slane = fq * 16 + fr;
;         f32x4 sv[8];
;         if (side) moe_item_load(*sp, side_layer, sit, slane, sv);
;         const int colj = u.pn * 128 + wc * 32 + 8 * fq;
;         const float* bg = b_up + u.e * 2048 + colj;
;         f32x4 bgv[2], blv[2];
; #pragma unroll
;         for (int n = 0; n < 2; ++n) { bgv[n] = *(const f32x4*)(bg + 4 * n); blv[n] = *(const f32x4*)(bg + 1024 + 4 * n); }
; #pragma unroll
;         for (int ai = 0; ai < 2; ++ai)
; #pragma unroll
;             for (int m = 0; m < 4; ++m) {
;                 const int row = u.pm + ai * 128 + wr * 64 + m * 16 + fr;
;                 float a[8];
; #pragma unroll
;                 for (int n = 0; n < 2; ++n)
; #pragma unroll
;                     for (int j = 0; j < 4; ++j) {
;                         const float g = fminf(acc[ai][0][m][n][j] + bgv[n][j], 7.f);
;                         const float l = fminf(fmaxf(acc[ai][1][m][n][j] + blv[n][j], -7.f), 7.f);
;                         const float sg = __builtin_amdgcn_rcpf(1.f + __builtin_amdgcn_exp2f(-1.702f * 1.4426950408889634f * g));
;                         a[n * 4 + j] = g * sg * (l + 1.f);
;                     }
;                 pg8::u32x4 w; w.x = pg8::cvt_pk_bf16(a[0], a[1]); w.y = pg8::cvt_pk_bf16(a[2], a[3]); w.z = pg8::cvt_pk_bf16(a[4], a[5]); w.w = pg8::cvt_pk_bf16(a[6], a[7]);
;                 *(pg8::u32x4*)(ACT + (size_t)row * 1024 + colj) = w;
;             }
.LBB0_1719:
	s_add_u32 s40, s36, 0xffffff00
	s_addc_u32 s41, s82, -1
	v_lshl_or_b32 v160, s47, 7, v149
	v_ashrrev_i32_e32 v161, 31, v160
	v_lshlrev_b64 v[160:161], 1, v[160:161]
	s_movk_i32 s33, 0x1dff
	s_and_b64 vcc, exec, s[44:45]
	s_cbranch_vccz .Lup_epi_nonext
	s_lshl_b32 s4, s52, 11
	s_ashr_i32 s5, s4, 31
	s_lshl_b64 s[4:5], s[4:5], 2
	v_lshl_or_b32 v136, s54, 7, v149
	s_add_u32 s4, s37, s4
	s_addc_u32 s5, s49, s5
	v_ashrrev_i32_e32 v137, 31, v136
	v_lshl_add_u64 v[136:137], v[136:137], 2, s[4:5]
	global_load_dwordx4 v[224:227], v[136:137], off
	global_load_dwordx4 v[228:231], v[136:137], off offset:16
	s_mov_b64 s[4:5], 0x1000
	v_lshl_add_u64 v[138:139], v[136:137], 0, s[4:5]
	global_load_dwordx4 v[232:235], v[138:139], off
	global_load_dwordx4 v[236:239], v[138:139], off offset:16
.Lup_epi_nonext:
	s_andn2_b64 vcc, exec, s[44:45]
	v_min_f32_e32 v2, 0x40e00000, v128
	v_mul_f32_e32 v155, 0xc01d265f, v2
	v_exp_f32_e32 v155, v155
	s_nop 0
	v_add_f32_e32 v155, 1.0, v155
	v_rcp_f32_e32 v155, v155
	v_med3_f32 v153, v96, s81, v222
	v_add_f32_e32 v153, 1.0, v153
	v_mul_f32_e32 v2, v2, v155
	v_mul_f32_e32 v2, v153, v2
	v_min_f32_e32 v153, 0x40e00000, v129
	v_mul_f32_e32 v182, 0xc01d265f, v153
	v_exp_f32_e32 v182, v182
	v_med3_f32 v155, v97, s81, v222
	v_add_f32_e32 v155, 1.0, v155
	v_add_f32_e32 v182, 1.0, v182
	v_rcp_f32_e32 v182, v182
	s_nop 0
	v_mul_f32_e32 v153, v153, v182
	v_mul_f32_e32 v153, v155, v153
	v_min_f32_e32 v155, 0x40e00000, v130
	v_mul_f32_e32 v183, 0xc01d265f, v155
	v_exp_f32_e32 v183, v183
	v_med3_f32 v182, v98, s81, v222
	v_add_f32_e32 v182, 1.0, v182
	v_add_f32_e32 v183, 1.0, v183
	v_rcp_f32_e32 v183, v183
	s_nop 0
	v_mul_f32_e32 v155, v155, v183
	v_mul_f32_e32 v155, v182, v155
	v_min_f32_e32 v182, 0x40e00000, v131
	v_mul_f32_e32 v184, 0xc01d265f, v182
	v_exp_f32_e32 v184, v184
	v_med3_f32 v183, v99, s81, v222
	v_add_f32_e32 v183, 1.0, v183
	v_add_f32_e32 v184, 1.0, v184
	v_rcp_f32_e32 v184, v184
	s_nop 0
	v_mul_f32_e32 v182, v182, v184
	v_mul_f32_e32 v182, v183, v182
	v_min_f32_e32 v183, 0x40e00000, v124
	v_mul_f32_e32 v185, 0xc01d265f, v183
	v_exp_f32_e32 v185, v185
	v_med3_f32 v184, v92, s81, v222
	v_add_f32_e32 v184, 1.0, v184
	v_add_f32_e32 v185, 1.0, v185
	v_rcp_f32_e32 v185, v185
	s_nop 0
	v_mul_f32_e32 v183, v183, v185
	v_mul_f32_e32 v183, v184, v183
	v_min_f32_e32 v184, 0x40e00000, v125
	v_mul_f32_e32 v186, 0xc01d265f, v184
	v_exp_f32_e32 v186, v186
	v_med3_f32 v185, v93, s81, v222
	v_add_f32_e32 v185, 1.0, v185
	v_add_f32_e32 v186, 1.0, v186
	v_rcp_f32_e32 v186, v186
	s_nop 0
	v_mul_f32_e32 v184, v184, v186
	v_mul_f32_e32 v186, v185, v184
	v_min_f32_e32 v184, 0x40e00000, v126
	v_mul_f32_e32 v187, 0xc01d265f, v184
	v_exp_f32_e32 v187, v187
	v_med3_f32 v185, v94, s81, v222
	v_add_f32_e32 v185, 1.0, v185
	v_add_f32_e32 v187, 1.0, v187
	v_rcp_f32_e32 v187, v187
	s_nop 0
	v_mul_f32_e32 v184, v184, v187
	v_mul_f32_e32 v187, v185, v184
	v_min_f32_e32 v184, 0x40e00000, v127
	v_mul_f32_e32 v188, 0xc01d265f, v184
	v_exp_f32_e32 v188, v188
	v_med3_f32 v185, v95, s81, v222
	v_add_f32_e32 v185, 1.0, v185
	v_add_f32_e32 v188, 1.0, v188
	v_rcp_f32_e32 v188, v188
	s_nop 0
	v_mul_f32_e32 v184, v184, v188
	v_mul_f32_e32 v189, v185, v184
	v_cvt_pk_bf16_f32 v184, v2, v153
	v_min_f32_e32 v2, 0x40e00000, v120
	v_cvt_pk_bf16_f32 v185, v155, v182
	v_mul_f32_e32 v155, 0xc01d265f, v2
	v_exp_f32_e32 v155, v155
	v_add_u32_e32 v188, s48, v169
	v_cvt_pk_bf16_f32 v186, v183, v186
	v_add_f32_e32 v155, 1.0, v155
	v_rcp_f32_e32 v155, v155
	v_cvt_pk_bf16_f32 v187, v187, v189
	v_ashrrev_i32_e32 v189, 31, v188
	v_med3_f32 v153, v88, s81, v222
	v_lshlrev_b64 v[182:183], 11, v[188:189]
	v_mul_f32_e32 v2, v2, v155
	v_add_f32_e32 v153, 1.0, v153
	v_lshl_add_u64 v[182:183], s[90:91], 0, v[182:183]
	v_mul_f32_e32 v2, v153, v2
	v_lshl_add_u64 v[182:183], v[182:183], 0, v[160:161]
	v_min_f32_e32 v153, 0x40e00000, v121
	global_store_dwordx4 v[182:183], v[184:187], off
	v_mul_f32_e32 v182, 0xc01d265f, v153
	v_exp_f32_e32 v182, v182
	v_med3_f32 v155, v89, s81, v222
	v_add_f32_e32 v155, 1.0, v155
	v_add_f32_e32 v182, 1.0, v182
	v_rcp_f32_e32 v182, v182
	s_nop 0
	v_mul_f32_e32 v153, v153, v182
	v_mul_f32_e32 v153, v155, v153
	v_min_f32_e32 v155, 0x40e00000, v122
	v_mul_f32_e32 v183, 0xc01d265f, v155
	v_exp_f32_e32 v183, v183
	v_med3_f32 v182, v90, s81, v222
	v_add_f32_e32 v182, 1.0, v182
	v_add_f32_e32 v183, 1.0, v183
	v_rcp_f32_e32 v183, v183
	s_nop 0
	v_mul_f32_e32 v155, v155, v183
	v_mul_f32_e32 v155, v182, v155
	v_min_f32_e32 v182, 0x40e00000, v123
	v_mul_f32_e32 v184, 0xc01d265f, v182
	v_exp_f32_e32 v184, v184
	v_med3_f32 v183, v91, s81, v222
	v_add_f32_e32 v183, 1.0, v183
	v_add_f32_e32 v184, 1.0, v184
	v_rcp_f32_e32 v184, v184
	s_nop 0
	v_mul_f32_e32 v182, v182, v184
	v_mul_f32_e32 v183, v183, v182
	v_min_f32_e32 v182, 0x40e00000, v116
	v_mul_f32_e32 v185, 0xc01d265f, v182
	v_exp_f32_e32 v185, v185
	v_med3_f32 v184, v84, s81, v222
	v_add_f32_e32 v184, 1.0, v184
	v_add_f32_e32 v185, 1.0, v185
	v_rcp_f32_e32 v185, v185
	s_nop 0
	v_mul_f32_e32 v182, v182, v185
	v_mul_f32_e32 v184, v184, v182
	v_min_f32_e32 v182, 0x40e00000, v117
	v_mul_f32_e32 v186, 0xc01d265f, v182
	v_exp_f32_e32 v186, v186
	v_med3_f32 v185, v85, s81, v222
	v_add_f32_e32 v185, 1.0, v185
	v_add_f32_e32 v186, 1.0, v186
	v_rcp_f32_e32 v186, v186
	s_nop 0
	v_mul_f32_e32 v182, v182, v186
	v_mul_f32_e32 v185, v185, v182
	v_min_f32_e32 v182, 0x40e00000, v118
	v_mul_f32_e32 v187, 0xc01d265f, v182
	v_exp_f32_e32 v187, v187
	v_med3_f32 v186, v86, s81, v222
	v_add_f32_e32 v186, 1.0, v186
	v_add_f32_e32 v187, 1.0, v187
	v_rcp_f32_e32 v187, v187
	s_nop 0
	v_mul_f32_e32 v182, v182, v187
; __device__ __forceinline__ unsigned cvt_pk_bf16(float lo, float hi) { unsigned r; asm volatile("v_cvt_pk_bf16_f32 %0, %1, %2" : "=v"(r) : "v"(lo), "v"(hi)); return r; }
;     __device__ __forceinline__ void operator()(const pg8::f32x4 (&acc)[2][2][4][2], const pg8::Unit& u, int wr, int wc, int fr, int fq) const {
;     ...
;         for (int ai = 0; ai < 2; ++ai)
; #pragma unroll
;             for (int m = 0; m < 4; ++m) {
;                 const int row = u.pm + ai * 128 + wr * 64 + m * 16 + fr;
;                 float a[8];
; #pragma unroll
;                 for (int n = 0; n < 2; ++n)
; #pragma unroll
;                     for (int j = 0; j < 4; ++j) {
;                         const float g = fminf(acc[ai][0][m][n][j] + bgv[n][j], 7.f);
;                         const float l = fminf(fmaxf(acc[ai][1][m][n][j] + blv[n][j], -7.f), 7.f);
;                         const float sg = __builtin_amdgcn_rcpf(1.f + __builtin_amdgcn_exp2f(-1.702f * 1.4426950408889634f * g));
;                         a[n * 4 + j] = g * sg * (l + 1.f);
;                     }
;                 pg8::u32x4 w; w.x = pg8::cvt_pk_bf16(a[0], a[1]); w.y = pg8::cvt_pk_bf16(a[2], a[3]); w.z = pg8::cvt_pk_bf16(a[4], a[5]); w.w = pg8::cvt_pk_bf16(a[6], a[7]);
;                 *(pg8::u32x4*)(ACT + (size_t)row * 1024 + colj) = w;
;             }
	v_mul_f32_e32 v187, v186, v182
	v_min_f32_e32 v182, 0x40e00000, v119
	v_mul_f32_e32 v188, 0xc01d265f, v182
	v_exp_f32_e32 v188, v188
	v_med3_f32 v186, v87, s81, v222
	v_add_f32_e32 v186, 1.0, v186
	v_add_f32_e32 v188, 1.0, v188
	v_rcp_f32_e32 v188, v188
	s_nop 0
	v_mul_f32_e32 v182, v182, v188
	v_mul_f32_e32 v188, v186, v182
	v_cvt_pk_bf16_f32 v182, v2, v153
	v_min_f32_e32 v2, 0x40e00000, v112
	v_cvt_pk_bf16_f32 v183, v155, v183
	v_mul_f32_e32 v155, 0xc01d265f, v2
	v_exp_f32_e32 v155, v155
	v_add_u32_e32 v186, s48, v151
	v_cvt_pk_bf16_f32 v184, v184, v185
	v_add_f32_e32 v155, 1.0, v155
	v_rcp_f32_e32 v155, v155
	v_cvt_pk_bf16_f32 v185, v187, v188
	v_ashrrev_i32_e32 v187, 31, v186
	v_med3_f32 v153, v80, s81, v222
	v_lshlrev_b64 v[186:187], 11, v[186:187]
	v_mul_f32_e32 v2, v2, v155
	v_add_f32_e32 v153, 1.0, v153
	v_lshl_add_u64 v[186:187], s[90:91], 0, v[186:187]
	v_mul_f32_e32 v2, v153, v2
	v_lshl_add_u64 v[186:187], v[186:187], 0, v[160:161]
	v_min_f32_e32 v153, 0x40e00000, v113
	global_store_dwordx4 v[186:187], v[182:185], off
	s_nop 1
	v_med3_f32 v155, v81, s81, v222
	v_mul_f32_e32 v182, 0xc01d265f, v153
	v_exp_f32_e32 v182, v182
	v_add_f32_e32 v155, 1.0, v155
	v_add_f32_e32 v182, 1.0, v182
	v_rcp_f32_e32 v182, v182
	s_nop 0
	v_mul_f32_e32 v153, v153, v182
	v_mul_f32_e32 v153, v155, v153
	v_min_f32_e32 v155, 0x40e00000, v114
	v_mul_f32_e32 v183, 0xc01d265f, v155
	v_exp_f32_e32 v183, v183
	v_med3_f32 v182, v82, s81, v222
	v_add_f32_e32 v182, 1.0, v182
	v_add_f32_e32 v183, 1.0, v183
	v_rcp_f32_e32 v183, v183
	s_nop 0
	v_mul_f32_e32 v155, v155, v183
	v_mul_f32_e32 v155, v182, v155
	v_min_f32_e32 v182, 0x40e00000, v115
	v_mul_f32_e32 v184, 0xc01d265f, v182
	v_exp_f32_e32 v184, v184
	v_med3_f32 v183, v83, s81, v222
	v_add_f32_e32 v183, 1.0, v183
	v_add_f32_e32 v184, 1.0, v184
	v_rcp_f32_e32 v184, v184
	s_nop 0
	v_mul_f32_e32 v182, v182, v184
	v_mul_f32_e32 v183, v183, v182
	v_min_f32_e32 v182, 0x40e00000, v108
	v_mul_f32_e32 v185, 0xc01d265f, v182
	v_exp_f32_e32 v185, v185
	v_med3_f32 v184, v76, s81, v222
	v_add_f32_e32 v184, 1.0, v184
	v_add_f32_e32 v185, 1.0, v185
	v_rcp_f32_e32 v185, v185
	s_nop 0
	v_mul_f32_e32 v182, v182, v185
	v_mul_f32_e32 v184, v184, v182
	v_min_f32_e32 v182, 0x40e00000, v109
	v_mul_f32_e32 v186, 0xc01d265f, v182
	v_exp_f32_e32 v186, v186
	v_med3_f32 v185, v77, s81, v222
	v_add_f32_e32 v185, 1.0, v185
	v_add_f32_e32 v186, 1.0, v186
	v_rcp_f32_e32 v186, v186
	s_nop 0
	v_mul_f32_e32 v182, v182, v186
	v_mul_f32_e32 v185, v185, v182
	v_min_f32_e32 v182, 0x40e00000, v110
	v_mul_f32_e32 v187, 0xc01d265f, v182
	v_exp_f32_e32 v187, v187
	v_med3_f32 v186, v78, s81, v222
	v_add_f32_e32 v186, 1.0, v186
	v_add_f32_e32 v187, 1.0, v187
	v_rcp_f32_e32 v187, v187
	s_nop 0
	v_mul_f32_e32 v182, v182, v187
	v_mul_f32_e32 v187, v186, v182
	v_min_f32_e32 v182, 0x40e00000, v111
	v_mul_f32_e32 v188, 0xc01d265f, v182
	v_exp_f32_e32 v188, v188
	v_med3_f32 v186, v79, s81, v222
	v_add_f32_e32 v186, 1.0, v186
	v_add_f32_e32 v188, 1.0, v188
	v_rcp_f32_e32 v188, v188
	s_nop 0
	v_mul_f32_e32 v182, v182, v188
	v_mul_f32_e32 v188, v186, v182
	v_cvt_pk_bf16_f32 v182, v2, v153
	v_min_f32_e32 v2, 0x40e00000, v104
	v_cvt_pk_bf16_f32 v183, v155, v183
	v_mul_f32_e32 v155, 0xc01d265f, v2
	v_exp_f32_e32 v155, v155
	v_add_u32_e32 v186, s48, v171
	v_cvt_pk_bf16_f32 v184, v184, v185
	v_add_f32_e32 v155, 1.0, v155
	v_rcp_f32_e32 v155, v155
	v_cvt_pk_bf16_f32 v185, v187, v188
	v_ashrrev_i32_e32 v187, 31, v186
	v_med3_f32 v153, v72, s81, v222
	v_lshlrev_b64 v[186:187], 11, v[186:187]
	v_mul_f32_e32 v2, v2, v155
	v_add_f32_e32 v153, 1.0, v153
	v_lshl_add_u64 v[186:187], s[90:91], 0, v[186:187]
	v_mul_f32_e32 v2, v153, v2
	v_lshl_add_u64 v[186:187], v[186:187], 0, v[160:161]
	v_min_f32_e32 v153, 0x40e00000, v105
	global_store_dwordx4 v[186:187], v[182:185], off
	s_nop 1
	v_med3_f32 v155, v73, s81, v222
	v_mul_f32_e32 v182, 0xc01d265f, v153
	v_exp_f32_e32 v182, v182
	v_add_f32_e32 v155, 1.0, v155
	v_add_f32_e32 v182, 1.0, v182
	v_rcp_f32_e32 v182, v182
	s_nop 0
	v_mul_f32_e32 v153, v153, v182
	v_mul_f32_e32 v153, v155, v153
	v_min_f32_e32 v155, 0x40e00000, v106
	v_mul_f32_e32 v183, 0xc01d265f, v155
	v_exp_f32_e32 v183, v183
	v_med3_f32 v182, v74, s81, v222
	v_add_f32_e32 v182, 1.0, v182
	v_add_f32_e32 v183, 1.0, v183
	v_rcp_f32_e32 v183, v183
	s_nop 0
	v_mul_f32_e32 v155, v155, v183
	v_mul_f32_e32 v155, v182, v155
	v_min_f32_e32 v182, 0x40e00000, v107
	v_mul_f32_e32 v184, 0xc01d265f, v182
	v_exp_f32_e32 v184, v184
	v_med3_f32 v183, v75, s81, v222
	v_add_f32_e32 v183, 1.0, v183
	v_add_f32_e32 v184, 1.0, v184
	v_rcp_f32_e32 v184, v184
	s_nop 0
	v_mul_f32_e32 v182, v182, v184
	v_mul_f32_e32 v183, v183, v182
	v_min_f32_e32 v182, 0x40e00000, v100
	v_mul_f32_e32 v185, 0xc01d265f, v182
	v_exp_f32_e32 v185, v185
	v_med3_f32 v184, v68, s81, v222
	v_add_f32_e32 v184, 1.0, v184
	v_add_f32_e32 v185, 1.0, v185
	v_rcp_f32_e32 v185, v185
	s_nop 0
	v_mul_f32_e32 v182, v182, v185
	v_mul_f32_e32 v184, v184, v182
	v_min_f32_e32 v182, 0x40e00000, v101
	v_mul_f32_e32 v186, 0xc01d265f, v182
	v_exp_f32_e32 v186, v186
	v_med3_f32 v185, v69, s81, v222
	v_add_f32_e32 v185, 1.0, v185
	v_add_f32_e32 v186, 1.0, v186
	v_rcp_f32_e32 v186, v186
	s_nop 0
	v_mul_f32_e32 v182, v182, v186
	v_mul_f32_e32 v185, v185, v182
	v_min_f32_e32 v182, 0x40e00000, v102
	v_mul_f32_e32 v187, 0xc01d265f, v182
	v_exp_f32_e32 v187, v187
	v_med3_f32 v186, v70, s81, v222
	v_add_f32_e32 v186, 1.0, v186
	v_add_f32_e32 v187, 1.0, v187
	v_rcp_f32_e32 v187, v187
	s_nop 0
	v_mul_f32_e32 v182, v182, v187
	v_mul_f32_e32 v187, v186, v182
	v_min_f32_e32 v182, 0x40e00000, v103
	v_mul_f32_e32 v188, 0xc01d265f, v182
; __device__ __forceinline__ unsigned cvt_pk_bf16(float lo, float hi) { unsigned r; asm volatile("v_cvt_pk_bf16_f32 %0, %1, %2" : "=v"(r) : "v"(lo), "v"(hi)); return r; }
;     __device__ __forceinline__ void operator()(const pg8::f32x4 (&acc)[2][2][4][2], const pg8::Unit& u, int wr, int wc, int fr, int fq) const {
;     ...
;         for (int ai = 0; ai < 2; ++ai)
; #pragma unroll
;             for (int m = 0; m < 4; ++m) {
;                 const int row = u.pm + ai * 128 + wr * 64 + m * 16 + fr;
;                 float a[8];
; #pragma unroll
;                 for (int n = 0; n < 2; ++n)
; #pragma unroll
;                     for (int j = 0; j < 4; ++j) {
;                         const float g = fminf(acc[ai][0][m][n][j] + bgv[n][j], 7.f);
;                         const float l = fminf(fmaxf(acc[ai][1][m][n][j] + blv[n][j], -7.f), 7.f);
;                         const float sg = __builtin_amdgcn_rcpf(1.f + __builtin_amdgcn_exp2f(-1.702f * 1.4426950408889634f * g));
;                         a[n * 4 + j] = g * sg * (l + 1.f);
;                     }
;                 pg8::u32x4 w; w.x = pg8::cvt_pk_bf16(a[0], a[1]); w.y = pg8::cvt_pk_bf16(a[2], a[3]); w.z = pg8::cvt_pk_bf16(a[4], a[5]); w.w = pg8::cvt_pk_bf16(a[6], a[7]);
;                 *(pg8::u32x4*)(ACT + (size_t)row * 1024 + colj) = w;
;             }
	v_exp_f32_e32 v188, v188
	v_med3_f32 v186, v71, s81, v222
	v_add_f32_e32 v186, 1.0, v186
	v_add_f32_e32 v188, 1.0, v188
	v_rcp_f32_e32 v188, v188
	s_nop 0
	v_mul_f32_e32 v182, v182, v188
	v_mul_f32_e32 v188, v186, v182
	v_cvt_pk_bf16_f32 v182, v2, v153
	v_min_f32_e32 v2, 0x40e00000, v64
	v_cvt_pk_bf16_f32 v183, v155, v183
	v_mul_f32_e32 v155, 0xc01d265f, v2
	v_exp_f32_e32 v155, v155
	v_add_u32_e32 v186, s48, v172
	v_cvt_pk_bf16_f32 v184, v184, v185
	v_add_f32_e32 v155, 1.0, v155
	v_rcp_f32_e32 v155, v155
	v_cvt_pk_bf16_f32 v185, v187, v188
	v_ashrrev_i32_e32 v187, 31, v186
	v_med3_f32 v153, v32, s81, v222
	v_lshlrev_b64 v[186:187], 11, v[186:187]
	v_mul_f32_e32 v2, v2, v155
	v_add_f32_e32 v153, 1.0, v153
	v_lshl_add_u64 v[186:187], s[90:91], 0, v[186:187]
	v_mul_f32_e32 v2, v153, v2
	v_lshl_add_u64 v[186:187], v[186:187], 0, v[160:161]
	v_min_f32_e32 v153, 0x40e00000, v65
	global_store_dwordx4 v[186:187], v[182:185], off
	s_nop 1
	v_med3_f32 v155, v33, s81, v222
	v_mul_f32_e32 v182, 0xc01d265f, v153
	v_exp_f32_e32 v182, v182
	v_add_f32_e32 v155, 1.0, v155
	v_add_f32_e32 v182, 1.0, v182
	v_rcp_f32_e32 v182, v182
	s_nop 0
	v_mul_f32_e32 v153, v153, v182
	v_mul_f32_e32 v153, v155, v153
	v_min_f32_e32 v155, 0x40e00000, v66
	v_mul_f32_e32 v183, 0xc01d265f, v155
	v_exp_f32_e32 v183, v183
	v_med3_f32 v182, v34, s81, v222
	v_add_f32_e32 v182, 1.0, v182
	v_add_f32_e32 v183, 1.0, v183
	v_rcp_f32_e32 v183, v183
	s_nop 0
	v_mul_f32_e32 v155, v155, v183
	v_mul_f32_e32 v155, v182, v155
	v_min_f32_e32 v182, 0x40e00000, v67
	v_mul_f32_e32 v184, 0xc01d265f, v182
	v_exp_f32_e32 v184, v184
	v_med3_f32 v183, v35, s81, v222
	v_add_f32_e32 v183, 1.0, v183
	v_add_f32_e32 v184, 1.0, v184
	v_rcp_f32_e32 v184, v184
	s_nop 0
	v_mul_f32_e32 v182, v182, v184
	v_mul_f32_e32 v183, v183, v182
	v_min_f32_e32 v182, 0x40e00000, v60
	v_mul_f32_e32 v185, 0xc01d265f, v182
	v_exp_f32_e32 v185, v185
	v_med3_f32 v184, v28, s81, v222
	v_add_f32_e32 v184, 1.0, v184
	v_add_f32_e32 v185, 1.0, v185
	v_rcp_f32_e32 v185, v185
	s_nop 0
	v_mul_f32_e32 v182, v182, v185
	v_mul_f32_e32 v184, v184, v182
	v_min_f32_e32 v182, 0x40e00000, v61
	v_mul_f32_e32 v186, 0xc01d265f, v182
	v_exp_f32_e32 v186, v186
	v_med3_f32 v185, v29, s81, v222
	v_add_f32_e32 v185, 1.0, v185
	v_add_f32_e32 v186, 1.0, v186
	v_rcp_f32_e32 v186, v186
	s_nop 0
	v_mul_f32_e32 v182, v182, v186
	v_mul_f32_e32 v185, v185, v182
	v_min_f32_e32 v182, 0x40e00000, v62
	v_mul_f32_e32 v187, 0xc01d265f, v182
	v_exp_f32_e32 v187, v187
	v_med3_f32 v186, v30, s81, v222
	v_add_f32_e32 v186, 1.0, v186
	v_add_f32_e32 v187, 1.0, v187
	v_rcp_f32_e32 v187, v187
	s_nop 0
	v_mul_f32_e32 v182, v182, v187
	v_mul_f32_e32 v187, v186, v182
	v_min_f32_e32 v182, 0x40e00000, v63
	v_mul_f32_e32 v188, 0xc01d265f, v182
	v_exp_f32_e32 v188, v188
	v_med3_f32 v186, v31, s81, v222
	v_add_f32_e32 v186, 1.0, v186
	v_add_f32_e32 v188, 1.0, v188
	v_rcp_f32_e32 v188, v188
	s_nop 0
	v_mul_f32_e32 v182, v182, v188
	v_mul_f32_e32 v188, v186, v182
	v_cvt_pk_bf16_f32 v182, v2, v153
	v_min_f32_e32 v2, 0x40e00000, v56
	v_cvt_pk_bf16_f32 v183, v155, v183
	v_mul_f32_e32 v155, 0xc01d265f, v2
	v_exp_f32_e32 v155, v155
	v_add_u32_e32 v186, s48, v173
	v_cvt_pk_bf16_f32 v184, v184, v185
	v_add_f32_e32 v155, 1.0, v155
	v_rcp_f32_e32 v155, v155
	v_cvt_pk_bf16_f32 v185, v187, v188
	v_ashrrev_i32_e32 v187, 31, v186
	v_med3_f32 v153, v24, s81, v222
	v_lshlrev_b64 v[186:187], 11, v[186:187]
	v_mul_f32_e32 v2, v2, v155
	v_add_f32_e32 v153, 1.0, v153
	v_lshl_add_u64 v[186:187], s[90:91], 0, v[186:187]
	v_mul_f32_e32 v2, v153, v2
	v_lshl_add_u64 v[186:187], v[186:187], 0, v[160:161]
	v_min_f32_e32 v153, 0x40e00000, v57
	global_store_dwordx4 v[186:187], v[182:185], off
	s_nop 1
	v_med3_f32 v155, v25, s81, v222
	v_mul_f32_e32 v182, 0xc01d265f, v153
	v_exp_f32_e32 v182, v182
	v_add_f32_e32 v155, 1.0, v155
	v_add_f32_e32 v182, 1.0, v182
	v_rcp_f32_e32 v182, v182
	s_nop 0
	v_mul_f32_e32 v153, v153, v182
	v_mul_f32_e32 v153, v155, v153
	v_min_f32_e32 v155, 0x40e00000, v58
	v_mul_f32_e32 v183, 0xc01d265f, v155
	v_exp_f32_e32 v183, v183
	v_med3_f32 v182, v26, s81, v222
	v_add_f32_e32 v182, 1.0, v182
	v_add_f32_e32 v183, 1.0, v183
	v_rcp_f32_e32 v183, v183
	s_nop 0
	v_mul_f32_e32 v155, v155, v183
	v_mul_f32_e32 v155, v182, v155
	v_min_f32_e32 v182, 0x40e00000, v59
	v_mul_f32_e32 v184, 0xc01d265f, v182
	v_exp_f32_e32 v184, v184
	v_med3_f32 v183, v27, s81, v222
	v_add_f32_e32 v183, 1.0, v183
	v_add_f32_e32 v184, 1.0, v184
	v_rcp_f32_e32 v184, v184
	s_nop 0
	v_mul_f32_e32 v182, v182, v184
	v_mul_f32_e32 v183, v183, v182
	v_min_f32_e32 v182, 0x40e00000, v52
	v_mul_f32_e32 v185, 0xc01d265f, v182
	v_exp_f32_e32 v185, v185
	v_med3_f32 v184, v20, s81, v222
	v_add_f32_e32 v184, 1.0, v184
	v_add_f32_e32 v185, 1.0, v185
	v_rcp_f32_e32 v185, v185
	s_nop 0
	v_mul_f32_e32 v182, v182, v185
	v_mul_f32_e32 v184, v184, v182
	v_min_f32_e32 v182, 0x40e00000, v53
	v_mul_f32_e32 v186, 0xc01d265f, v182
	v_exp_f32_e32 v186, v186
	v_med3_f32 v185, v21, s81, v222
	v_add_f32_e32 v185, 1.0, v185
	v_add_f32_e32 v186, 1.0, v186
	v_rcp_f32_e32 v186, v186
	s_nop 0
	v_mul_f32_e32 v182, v182, v186
	v_mul_f32_e32 v185, v185, v182
	v_min_f32_e32 v182, 0x40e00000, v54
	v_mul_f32_e32 v187, 0xc01d265f, v182
	v_exp_f32_e32 v187, v187
	v_med3_f32 v186, v22, s81, v222
	v_add_f32_e32 v186, 1.0, v186
	v_add_f32_e32 v187, 1.0, v187
	v_rcp_f32_e32 v187, v187
	s_nop 0
	v_mul_f32_e32 v182, v182, v187
	v_mul_f32_e32 v187, v186, v182
	v_min_f32_e32 v182, 0x40e00000, v55
	v_mul_f32_e32 v188, 0xc01d265f, v182
	v_exp_f32_e32 v188, v188
	v_med3_f32 v186, v23, s81, v222
	v_add_f32_e32 v186, 1.0, v186
	v_add_f32_e32 v188, 1.0, v188
; __device__ __forceinline__ unsigned cvt_pk_bf16(float lo, float hi) { unsigned r; asm volatile("v_cvt_pk_bf16_f32 %0, %1, %2" : "=v"(r) : "v"(lo), "v"(hi)); return r; }
; template <class Epi, class Sched, bool ALIGN_EPI = false, bool SP2 = false, bool GATHER = false, bool HALFM = false>
; __device__ __forceinline__ void gemm_phase(PG8_LAS unsigned char* lds, const int Kdim, const Sched& S, const Epi& E) {
;     ...
;         if (!has_next) break;
;     __device__ __forceinline__ void operator()(const pg8::f32x4 (&acc)[2][2][4][2], const pg8::Unit& u, int wr, int wc, int fr, int fq) const {
;     ...
;         for (int ai = 0; ai < 2; ++ai)
; #pragma unroll
;             for (int m = 0; m < 4; ++m) {
;                 const int row = u.pm + ai * 128 + wr * 64 + m * 16 + fr;
;                 float a[8];
; #pragma unroll
;                 for (int n = 0; n < 2; ++n)
; #pragma unroll
;                     for (int j = 0; j < 4; ++j) {
;                         const float g = fminf(acc[ai][0][m][n][j] + bgv[n][j], 7.f);
;                         const float l = fminf(fmaxf(acc[ai][1][m][n][j] + blv[n][j], -7.f), 7.f);
;                         const float sg = __builtin_amdgcn_rcpf(1.f + __builtin_amdgcn_exp2f(-1.702f * 1.4426950408889634f * g));
;                         a[n * 4 + j] = g * sg * (l + 1.f);
;                     }
;                 pg8::u32x4 w; w.x = pg8::cvt_pk_bf16(a[0], a[1]); w.y = pg8::cvt_pk_bf16(a[2], a[3]); w.z = pg8::cvt_pk_bf16(a[4], a[5]); w.w = pg8::cvt_pk_bf16(a[6], a[7]);
;                 *(pg8::u32x4*)(ACT + (size_t)row * 1024 + colj) = w;
;             }
	v_rcp_f32_e32 v188, v188
	s_nop 0
	v_mul_f32_e32 v182, v182, v188
	v_mul_f32_e32 v188, v186, v182
	v_cvt_pk_bf16_f32 v182, v2, v153
	v_min_f32_e32 v2, 0x40e00000, v48
	v_cvt_pk_bf16_f32 v183, v155, v183
	v_mul_f32_e32 v155, 0xc01d265f, v2
	v_exp_f32_e32 v155, v155
	v_add_u32_e32 v186, s48, v174
	v_cvt_pk_bf16_f32 v184, v184, v185
	v_add_f32_e32 v155, 1.0, v155
	v_rcp_f32_e32 v155, v155
	v_cvt_pk_bf16_f32 v185, v187, v188
	v_ashrrev_i32_e32 v187, 31, v186
	v_med3_f32 v153, v16, s81, v222
	v_lshlrev_b64 v[186:187], 11, v[186:187]
	v_mul_f32_e32 v2, v2, v155
	v_add_f32_e32 v153, 1.0, v153
	v_lshl_add_u64 v[186:187], s[90:91], 0, v[186:187]
	v_mul_f32_e32 v2, v153, v2
	v_lshl_add_u64 v[186:187], v[186:187], 0, v[160:161]
	v_min_f32_e32 v153, 0x40e00000, v49
	global_store_dwordx4 v[186:187], v[182:185], off
	s_nop 1
	v_med3_f32 v155, v17, s81, v222
	v_mul_f32_e32 v182, 0xc01d265f, v153
	v_exp_f32_e32 v182, v182
	v_add_f32_e32 v155, 1.0, v155
	v_add_f32_e32 v182, 1.0, v182
	v_rcp_f32_e32 v182, v182
	s_nop 0
	v_mul_f32_e32 v153, v153, v182
	v_mul_f32_e32 v153, v155, v153
	v_min_f32_e32 v155, 0x40e00000, v50
	v_mul_f32_e32 v183, 0xc01d265f, v155
	v_exp_f32_e32 v183, v183
	v_med3_f32 v182, v18, s81, v222
	v_add_f32_e32 v182, 1.0, v182
	v_add_f32_e32 v183, 1.0, v183
	v_rcp_f32_e32 v183, v183
	s_nop 0
	v_mul_f32_e32 v155, v155, v183
	v_mul_f32_e32 v155, v182, v155
	v_min_f32_e32 v182, 0x40e00000, v51
	v_mul_f32_e32 v184, 0xc01d265f, v182
	v_exp_f32_e32 v184, v184
	v_med3_f32 v183, v19, s81, v222
	v_add_f32_e32 v183, 1.0, v183
	v_add_f32_e32 v184, 1.0, v184
	v_rcp_f32_e32 v184, v184
	s_nop 0
	v_mul_f32_e32 v182, v182, v184
	v_mul_f32_e32 v183, v183, v182
	v_min_f32_e32 v182, 0x40e00000, v44
	v_mul_f32_e32 v185, 0xc01d265f, v182
	v_exp_f32_e32 v185, v185
	v_med3_f32 v184, v12, s81, v222
	v_add_f32_e32 v184, 1.0, v184
	v_add_f32_e32 v185, 1.0, v185
	v_rcp_f32_e32 v185, v185
	v_min_f32_e32 v132, 0x40e00000, v36
	v_mul_f32_e32 v182, v182, v185
	v_mul_f32_e32 v184, v184, v182
	v_min_f32_e32 v182, 0x40e00000, v45
	v_mul_f32_e32 v186, 0xc01d265f, v182
	v_exp_f32_e32 v186, v186
	v_med3_f32 v185, v13, s81, v222
	v_add_f32_e32 v185, 1.0, v185
	v_add_f32_e32 v186, 1.0, v186
	v_rcp_f32_e32 v186, v186
	v_med3_f32 v136, v4, s81, v222
	v_add_f32_e32 v136, 1.0, v136
	v_mul_f32_e32 v182, v182, v186
	v_mul_f32_e32 v185, v185, v182
	v_min_f32_e32 v182, 0x40e00000, v46
	v_mul_f32_e32 v187, 0xc01d265f, v182
	v_exp_f32_e32 v187, v187
	v_med3_f32 v186, v14, s81, v222
	v_add_f32_e32 v186, 1.0, v186
	v_add_f32_e32 v187, 1.0, v187
	v_rcp_f32_e32 v187, v187
	s_nop 0
	v_mul_f32_e32 v182, v182, v187
	v_mul_f32_e32 v187, v186, v182
	v_min_f32_e32 v182, 0x40e00000, v47
	v_mul_f32_e32 v188, 0xc01d265f, v182
	v_exp_f32_e32 v188, v188
	v_med3_f32 v186, v15, s81, v222
	v_add_f32_e32 v186, 1.0, v186
	v_add_f32_e32 v188, 1.0, v188
	v_rcp_f32_e32 v188, v188
	s_nop 0
	v_mul_f32_e32 v182, v182, v188
	v_mul_f32_e32 v188, v186, v182
	v_cvt_pk_bf16_f32 v182, v2, v153
	v_min_f32_e32 v2, 0x40e00000, v40
	v_mul_f32_e32 v144, 0xc01d265f, v2
	v_exp_f32_e32 v144, v144
	v_med3_f32 v140, v8, s81, v222
	v_add_f32_e32 v140, 1.0, v140
	v_add_u32_e32 v186, s48, v175
	v_add_f32_e32 v144, 1.0, v144
	v_rcp_f32_e32 v144, v144
	v_cvt_pk_bf16_f32 v183, v155, v183
	v_cvt_pk_bf16_f32 v184, v184, v185
	v_cvt_pk_bf16_f32 v185, v187, v188
	v_ashrrev_i32_e32 v187, 31, v186
	v_mul_f32_e32 v2, v2, v144
	v_mul_f32_e32 v2, v140, v2
	v_min_f32_e32 v140, 0x40e00000, v41
	v_mul_f32_e32 v144, 0xc01d265f, v140
	v_exp_f32_e32 v144, v144
	v_med3_f32 v141, v9, s81, v222
	v_add_f32_e32 v141, 1.0, v141
	v_add_f32_e32 v144, 1.0, v144
	v_rcp_f32_e32 v144, v144
	v_lshlrev_b64 v[186:187], 11, v[186:187]
	v_lshl_add_u64 v[186:187], s[90:91], 0, v[186:187]
	v_lshl_add_u64 v[186:187], v[186:187], 0, v[160:161]
	v_mul_f32_e32 v140, v140, v144
	v_mul_f32_e32 v140, v141, v140
	v_min_f32_e32 v141, 0x40e00000, v42
	v_mul_f32_e32 v144, 0xc01d265f, v141
	v_exp_f32_e32 v144, v144
	v_med3_f32 v142, v10, s81, v222
	v_add_f32_e32 v142, 1.0, v142
	v_add_f32_e32 v144, 1.0, v144
	v_rcp_f32_e32 v144, v144
	global_store_dwordx4 v[186:187], v[182:185], off
	v_mul_f32_e32 v141, v141, v144
	v_mul_f32_e32 v141, v142, v141
	v_min_f32_e32 v142, 0x40e00000, v43
	v_mul_f32_e32 v144, 0xc01d265f, v142
	v_exp_f32_e32 v144, v144
	v_med3_f32 v143, v11, s81, v222
	v_add_f32_e32 v143, 1.0, v143
	v_add_f32_e32 v144, 1.0, v144
	v_rcp_f32_e32 v144, v144
	s_nop 0
	v_mul_f32_e32 v142, v142, v144
	v_mul_f32_e32 v142, v143, v142
	v_mul_f32_e32 v143, 0xc01d265f, v132
	v_exp_f32_e32 v143, v143
	s_nop 0
	v_add_f32_e32 v143, 1.0, v143
	v_rcp_f32_e32 v143, v143
	s_nop 0
	v_mul_f32_e32 v132, v132, v143
	v_mul_f32_e32 v143, v136, v132
	v_min_f32_e32 v132, 0x40e00000, v37
	v_mul_f32_e32 v136, 0xc01d265f, v132
	v_exp_f32_e32 v136, v136
	v_med3_f32 v133, v5, s81, v222
	v_add_f32_e32 v133, 1.0, v133
	v_add_f32_e32 v136, 1.0, v136
	v_rcp_f32_e32 v136, v136
	s_nop 0
	v_mul_f32_e32 v132, v132, v136
	v_mul_f32_e32 v137, v133, v132
	v_min_f32_e32 v132, 0x40e00000, v38
	v_mul_f32_e32 v134, 0xc01d265f, v132
	v_exp_f32_e32 v134, v134
	v_med3_f32 v133, v6, s81, v222
	v_add_f32_e32 v133, 1.0, v133
	v_add_f32_e32 v134, 1.0, v134
	v_rcp_f32_e32 v134, v134
	v_add_u32_e32 v136, s48, v176
	v_mul_f32_e32 v132, v132, v134
	v_mul_f32_e32 v138, v133, v132
	v_min_f32_e32 v132, 0x40e00000, v39
	v_mul_f32_e32 v134, 0xc01d265f, v132
	v_exp_f32_e32 v134, v134
	v_med3_f32 v133, v7, s81, v222
	v_add_f32_e32 v133, 1.0, v133
	v_add_f32_e32 v134, 1.0, v134
	v_rcp_f32_e32 v134, v134
	s_nop 0
	v_mul_f32_e32 v132, v132, v134
	v_mul_f32_e32 v135, v133, v132
	v_cvt_pk_bf16_f32 v132, v2, v140
	v_cvt_pk_bf16_f32 v133, v141, v142
	v_cvt_pk_bf16_f32 v134, v143, v137
	v_ashrrev_i32_e32 v137, 31, v136
	v_lshlrev_b64 v[136:137], 11, v[136:137]
	v_lshl_add_u64 v[136:137], s[90:91], 0, v[136:137]
	v_lshl_add_u64 v[136:137], v[136:137], 0, v[160:161]
	v_cvt_pk_bf16_f32 v135, v138, v135
	global_store_dwordx4 v[136:137], v[132:135], off
	s_cbranch_vccnz .LBB0_1722
	v_readlane_b32 s82, v255, 1
	v_readlane_b32 s83, v255, 2
	s_branch .LBB0_1697
